# sc1 write-through on the QKV epilogue stores (Q/K/V/LF) + final RMSNorm rewrite with sc1 output stores
# speedup vs baseline: 1.0042x; 1.0037x over previous
.LBB0_1850:
	v_mov_b32_e32 v171, v0
	s_lshl_b32 s15, s18, 8
	v_readfirstlane_b32 s10, v171
	s_ashr_i32 s76, s10, 8
	s_lshl_b32 s13, s76, 6
	v_and_b32_e32 v170, 63, v171
	s_add_i32 s78, s13, s15
	v_or_b32_e32 v130, s78, v170
	v_ashrrev_i32_e32 v131, 31, v130
	v_lshl_add_u64 v[130:131], v[130:131], 2, s[22:23]
	v_add_co_u32_e32 v132, vcc, s70, v130
	global_load_dword v134, v[130:131], off
	s_nop 0
	v_addc_co_u32_e32 v133, vcc, 0, v131, vcc
	global_load_dword v135, v[132:133], off
	v_add_co_u32_e32 v132, vcc, s71, v130
	s_ashr_i32 s10, s10, 6
	s_nop 0
	v_addc_co_u32_e32 v133, vcc, 0, v131, vcc
	global_load_dword v136, v[132:133], off
	v_add_co_u32_e32 v132, vcc, s58, v130
	s_mul_i32 s11, s10, 0xb00
	s_nop 0
	v_addc_co_u32_e32 v133, vcc, 0, v131, vcc
	global_load_dword v137, v[132:133], off
	v_add_co_u32_e32 v132, vcc, s59, v130
	s_add_i32 s19, s11, 0
	s_nop 0
	v_addc_co_u32_e32 v133, vcc, 0, v131, vcc
	global_load_dword v138, v[132:133], off
	v_add_co_u32_e32 v132, vcc, s56, v130
	s_add_i32 s19, s19, 0x20000
	s_nop 0
	v_addc_co_u32_e32 v133, vcc, 0, v131, vcc
	global_load_dword v139, v[132:133], off
	v_add_co_u32_e32 v132, vcc, s97, v130
	s_or_b32 s14, s15, 0x80
	s_nop 0
	v_addc_co_u32_e32 v133, vcc, 0, v131, vcc
	global_load_dword v140, v[132:133], off
	v_add_co_u32_e32 v132, vcc, s4, v130
	s_add_i32 s80, s13, s14
	s_nop 0
	v_addc_co_u32_e32 v133, vcc, 0, v131, vcc
	global_load_dword v141, v[132:133], off
	v_add_co_u32_e32 v132, vcc, s5, v130
	s_and_b32 s49, s10, 3
	s_nop 0
	v_addc_co_u32_e32 v133, vcc, 0, v131, vcc
	global_load_dword v142, v[132:133], off
	v_add_co_u32_e32 v132, vcc, s54, v130
	v_and_b32_e32 v172, 15, v171
	s_nop 0
	v_addc_co_u32_e32 v133, vcc, 0, v131, vcc
	global_load_dword v143, v[132:133], off
	v_add_co_u32_e32 v132, vcc, s55, v130
	s_cmp_gt_i32 s12, 11
	s_nop 0
	v_addc_co_u32_e32 v133, vcc, 0, v131, vcc
	global_load_dword v144, v[132:133], off
	v_add_co_u32_e32 v132, vcc, s61, v130
	s_mov_b64 s[10:11], -1
	s_nop 0
	v_addc_co_u32_e32 v133, vcc, 0, v131, vcc
	global_load_dword v145, v[132:133], off
	v_add_co_u32_e32 v132, vcc, s1, v130
	s_nop 1
	v_addc_co_u32_e32 v133, vcc, 0, v131, vcc
	global_load_dword v154, v[132:133], off
	v_add_co_u32_e32 v132, vcc, s0, v130
	s_nop 1
	v_addc_co_u32_e32 v133, vcc, 0, v131, vcc
	global_load_dword v160, v[132:133], off
	v_add_co_u32_e32 v132, vcc, s62, v130
	s_nop 1
	v_addc_co_u32_e32 v133, vcc, 0, v131, vcc
	v_add_co_u32_e32 v130, vcc, s94, v130
	global_load_dword v132, v[132:133], off
	s_nop 0
	v_addc_co_u32_e32 v131, vcc, 0, v131, vcc
	global_load_dword v130, v[130:131], off
	s_waitcnt vmcnt(0)
	v_add_f32_e32 v131, v134, v135
	v_add_f32_e32 v133, v136, v137
	v_add_f32_e32 v131, v131, v133
	v_add_f32_e32 v134, v138, v139
	v_add_f32_e32 v133, v140, v141
	v_add_f32_e32 v133, v134, v133
	v_add_f32_e32 v131, v131, v133
	v_add_f32_e32 v133, v142, v143
	v_add_f32_e32 v134, v144, v145
	v_add_f32_e32 v133, v133, v134
	v_add_f32_e32 v134, v154, v160
	v_add_f32_e32 v130, v132, v130
	v_add_f32_e32 v130, v134, v130
	v_add_f32_e32 v130, v133, v130
	v_add_f32_e32 v130, v131, v130
	v_fmamk_f32 v130, v130, 0x3a800000, v167
	v_rsq_f32_e32 v130, v130
	v_lshl_add_u32 v134, v170, 2, s19
	ds_write_b32 v134, v130 offset:2304
	v_or_b32_e32 v130, s80, v170
	v_ashrrev_i32_e32 v131, 31, v130
	v_lshl_add_u64 v[130:131], v[130:131], 2, s[22:23]
	v_add_co_u32_e32 v132, vcc, s70, v130
	global_load_dword v135, v[130:131], off
	s_nop 0
	v_addc_co_u32_e32 v133, vcc, 0, v131, vcc
	global_load_dword v136, v[132:133], off
	v_add_co_u32_e32 v132, vcc, s71, v130
	s_nop 1
	v_addc_co_u32_e32 v133, vcc, 0, v131, vcc
	global_load_dword v137, v[132:133], off
	v_add_co_u32_e32 v132, vcc, s58, v130
	s_nop 1
	v_addc_co_u32_e32 v133, vcc, 0, v131, vcc
	global_load_dword v138, v[132:133], off
	v_add_co_u32_e32 v132, vcc, s59, v130
	s_nop 1
	v_addc_co_u32_e32 v133, vcc, 0, v131, vcc
	global_load_dword v139, v[132:133], off
	v_add_co_u32_e32 v132, vcc, s56, v130
	s_nop 1
	v_addc_co_u32_e32 v133, vcc, 0, v131, vcc
	global_load_dword v140, v[132:133], off
	v_add_co_u32_e32 v132, vcc, s97, v130
	s_nop 1
	v_addc_co_u32_e32 v133, vcc, 0, v131, vcc
	global_load_dword v141, v[132:133], off
	v_add_co_u32_e32 v132, vcc, s4, v130
	s_nop 1
	v_addc_co_u32_e32 v133, vcc, 0, v131, vcc
	global_load_dword v142, v[132:133], off
	v_add_co_u32_e32 v132, vcc, s5, v130
	s_nop 1
	v_addc_co_u32_e32 v133, vcc, 0, v131, vcc
	global_load_dword v143, v[132:133], off
	v_add_co_u32_e32 v132, vcc, s54, v130
	s_nop 1
	v_addc_co_u32_e32 v133, vcc, 0, v131, vcc
	global_load_dword v144, v[132:133], off
	v_add_co_u32_e32 v132, vcc, s55, v130
	s_nop 1
	v_addc_co_u32_e32 v133, vcc, 0, v131, vcc
	global_load_dword v145, v[132:133], off
	v_add_co_u32_e32 v132, vcc, s61, v130
	s_nop 1
	v_addc_co_u32_e32 v133, vcc, 0, v131, vcc
	global_load_dword v154, v[132:133], off
	v_add_co_u32_e32 v132, vcc, s1, v130
	s_nop 1
	v_addc_co_u32_e32 v133, vcc, 0, v131, vcc
	global_load_dword v160, v[132:133], off
	v_add_co_u32_e32 v132, vcc, s0, v130
	s_nop 1
	v_addc_co_u32_e32 v133, vcc, 0, v131, vcc
	global_load_dword v161, v[132:133], off
	v_add_co_u32_e32 v132, vcc, s62, v130
	s_nop 1
	v_addc_co_u32_e32 v133, vcc, 0, v131, vcc
	v_add_co_u32_e32 v130, vcc, s94, v130
	global_load_dword v132, v[132:133], off
	s_nop 0
	v_addc_co_u32_e32 v131, vcc, 0, v131, vcc
	global_load_dword v130, v[130:131], off
	s_waitcnt vmcnt(0)
	v_add_f32_e32 v131, v135, v136
	v_add_f32_e32 v133, v137, v138
	v_add_f32_e32 v131, v131, v133
	v_add_f32_e32 v133, v139, v140
	v_add_f32_e32 v135, v141, v142
	v_add_f32_e32 v133, v133, v135
	v_add_f32_e32 v131, v131, v133
	v_add_f32_e32 v133, v143, v144
	v_add_f32_e32 v135, v145, v154
	v_add_f32_e32 v133, v133, v135
	v_add_f32_e32 v135, v160, v161
	v_add_f32_e32 v130, v132, v130
	v_add_f32_e32 v130, v135, v130
	v_add_f32_e32 v130, v133, v130
	v_add_f32_e32 v130, v131, v130
	v_fmamk_f32 v130, v130, 0x3a800000, v167
	v_rsq_f32_e32 v130, v130
	ds_write_b32 v134, v130 offset:2560
	s_cbranch_scc0 .LBB0_1854
	s_cmp_eq_u32 s49, 0
	s_cselect_b64 s[10:11], -1, 0
	v_cmp_gt_u32_e32 vcc, 32, v170
	s_and_b64 s[16:17], s[10:11], vcc
	s_and_saveexec_b64 s[10:11], s[16:17]
	s_cbranch_execz .LBB0_1853
	v_lshlrev_b32_e32 v130, 1, v171
	v_readlane_b32 s16, v254, 30
	v_and_b32_e32 v154, 32, v130
	v_readlane_b32 s17, v254, 31
	s_nop 4
	global_load_dwordx4 v[130:133], v154, s[16:17]
	global_load_dwordx4 v[134:137], v154, s[16:17] offset:16
	v_lshl_add_u32 v138, v172, 2, s19
	v_add_u32_e32 v173, 0x800, v138
	ds_read2_b32 v[162:163], v173 offset0:64 offset1:80
	s_waitcnt lgkmcnt(0)
	v_mul_f32_e32 v142, 0x3d800000, v162
	s_waitcnt vmcnt(0)
	v_pk_fma_f32 v[140:141], v[122:123], v[142:143], v[134:135] op_sel_hi:[1,0,1]
	s_nop 0
	v_min_f32_e32 v144, 0, v140
	v_mul_f32_e64 v140, |v140|, s33
	v_exp_f32_e32 v140, v140
	v_pk_fma_f32 v[138:139], v[124:125], v[142:143], v[136:137] op_sel_hi:[1,0,1]
	v_min_f32_e32 v145, 0, v141
	v_add_f32_e32 v140, 1.0, v140
	v_log_f32_e32 v143, v140
	v_mul_f32_e64 v140, |v141|, s33
	v_exp_f32_e32 v140, v140
	v_min_f32_e32 v141, 0, v139
	v_mul_f32_e64 v139, |v139|, s33
	v_exp_f32_e32 v139, v139
	v_add_f32_e32 v140, 1.0, v140
	v_log_f32_e32 v160, v140
	v_min_f32_e32 v140, 0, v138
	v_mul_f32_e64 v138, |v138|, s33
	v_exp_f32_e32 v138, v138
	v_add_f32_e32 v139, 1.0, v139
	v_log_f32_e32 v139, v139
	v_add_f32_e32 v138, 1.0, v138
	v_log_f32_e32 v138, v138
	v_xor_b32_e32 v139, 0x80000000, v139
	v_xor_b32_e32 v138, 0x80000000, v138
	v_pk_fma_f32 v[140:141], v[138:139], s[46:47], v[140:141] op_sel_hi:[1,0,1]
	v_xor_b32_e32 v139, 0x80000000, v160
	v_xor_b32_e32 v138, 0x80000000, v143
	v_pk_fma_f32 v[138:139], v[138:139], s[46:47], v[144:145] op_sel_hi:[1,0,1]
	v_pk_fma_f32 v[144:145], v[128:129], v[142:143], v[132:133] op_sel_hi:[1,0,1]
	v_pk_fma_f32 v[142:143], v[126:127], v[142:143], v[130:131] op_sel_hi:[1,0,1]
	s_nop 0
	v_min_f32_e32 v160, 0, v142
	v_mul_f32_e64 v142, |v142|, s33
	v_exp_f32_e32 v142, v142
	v_min_f32_e32 v161, 0, v143
	v_add_f32_e32 v142, 1.0, v142
	v_log_f32_e32 v162, v142
	v_mul_f32_e64 v142, |v143|, s33
	v_mul_f32_e64 v143, |v144|, s33
	v_exp_f32_e32 v142, v142
	v_exp_f32_e32 v143, v143
	v_add_f32_e32 v142, 1.0, v142
	v_add_f32_e32 v143, 1.0, v143
	v_log_f32_e32 v174, v142
	v_min_f32_e32 v142, 0, v144
	v_log_f32_e32 v144, v143
	v_min_f32_e32 v143, 0, v145
	v_mul_f32_e64 v145, |v145|, s33
	v_exp_f32_e32 v145, v145
	v_xor_b32_e32 v144, 0x80000000, v144
	v_add_f32_e32 v145, 1.0, v145
	v_log_f32_e32 v145, v145
	s_nop 0
	v_xor_b32_e32 v145, 0x80000000, v145
	v_pk_fma_f32 v[144:145], v[144:145], s[46:47], v[142:143] op_sel_hi:[1,0,1]
	v_xor_b32_e32 v143, 0x80000000, v174
	v_xor_b32_e32 v142, 0x80000000, v162
	v_pk_fma_f32 v[142:143], v[142:143], s[46:47], v[160:161] op_sel_hi:[1,0,1]
	v_or_b32_e32 v160, s15, v172
	v_add_u32_e32 v160, s13, v160
	v_ashrrev_i32_e32 v161, 31, v160
	v_lshlrev_b64 v[174:175], 6, v[160:161]
	v_lshl_add_u64 v[174:175], s[24:25], 0, v[174:175]
	v_lshl_add_u64 v[174:175], v[174:175], 0, v[154:155]
	global_store_dwordx4 v[174:175], v[142:145], off sc1
	global_store_dwordx4 v[174:175], v[138:141], off offset:16 sc1
	s_nop 1
	v_mul_f32_e32 v138, 0x3d800000, v163
	v_pk_fma_f32 v[144:145], v[106:107], v[138:139], v[134:135] op_sel_hi:[1,0,1]
	v_pk_fma_f32 v[142:143], v[108:109], v[138:139], v[136:137] op_sel_hi:[1,0,1]
	v_min_f32_e32 v140, 0, v144
	v_mul_f32_e64 v139, |v144|, s33
	v_mul_f32_e64 v144, |v145|, s33
	v_exp_f32_e32 v144, v144
	v_min_f32_e32 v141, 0, v145
	v_min_f32_e32 v145, 0, v143
	v_mul_f32_e64 v143, |v143|, s33
	v_add_f32_e32 v144, 1.0, v144
	v_log_f32_e32 v161, v144
	v_min_f32_e32 v144, 0, v142
	v_mul_f32_e64 v142, |v142|, s33
	v_exp_f32_e32 v142, v142
	v_exp_f32_e32 v143, v143
	v_exp_f32_e32 v139, v139
	v_add_f32_e32 v142, 1.0, v142
	v_add_f32_e32 v143, 1.0, v143
	v_add_f32_e32 v139, 1.0, v139
	v_log_f32_e32 v142, v142
	v_log_f32_e32 v143, v143
	v_log_f32_e32 v139, v139
	v_xor_b32_e32 v142, 0x80000000, v142
	v_xor_b32_e32 v143, 0x80000000, v143
	v_pk_fma_f32 v[142:143], v[142:143], s[46:47], v[144:145] op_sel_hi:[1,0,1]
	v_xor_b32_e32 v145, 0x80000000, v161
	v_xor_b32_e32 v144, 0x80000000, v139
	v_pk_fma_f32 v[140:141], v[144:145], s[46:47], v[140:141] op_sel_hi:[1,0,1]
	v_pk_fma_f32 v[144:145], v[112:113], v[138:139], v[132:133] op_sel_hi:[1,0,1]
	v_pk_fma_f32 v[138:139], v[110:111], v[138:139], v[130:131] op_sel_hi:[1,0,1]
	s_nop 0
	v_min_f32_e32 v162, 0, v138
	v_mul_f32_e64 v138, |v138|, s33
	v_exp_f32_e32 v138, v138
	v_min_f32_e32 v163, 0, v139
	v_add_f32_e32 v138, 1.0, v138
	v_log_f32_e32 v161, v138
	v_mul_f32_e64 v138, |v139|, s33
	v_mul_f32_e64 v139, |v144|, s33
	v_exp_f32_e32 v138, v138
	v_exp_f32_e32 v139, v139
	v_add_f32_e32 v138, 1.0, v138
	v_add_f32_e32 v139, 1.0, v139
	v_log_f32_e32 v174, v138
	v_min_f32_e32 v138, 0, v144
	v_log_f32_e32 v144, v139
	v_min_f32_e32 v139, 0, v145
	v_mul_f32_e64 v145, |v145|, s33
	v_exp_f32_e32 v145, v145
	v_xor_b32_e32 v144, 0x80000000, v144
	v_add_f32_e32 v145, 1.0, v145
	v_log_f32_e32 v145, v145
	s_nop 0
	v_xor_b32_e32 v145, 0x80000000, v145
	v_pk_fma_f32 v[176:177], v[144:145], s[46:47], v[138:139] op_sel_hi:[1,0,1]
	v_xor_b32_e32 v139, 0x80000000, v174
	v_xor_b32_e32 v138, 0x80000000, v161
	v_pk_fma_f32 v[174:175], v[138:139], s[46:47], v[162:163] op_sel_hi:[1,0,1]
	v_add_u32_e32 v138, 16, v160
	v_ashrrev_i32_e32 v139, 31, v138
	v_lshlrev_b64 v[138:139], 6, v[138:139]
	v_lshl_add_u64 v[138:139], s[24:25], 0, v[138:139]
	v_lshl_add_u64 v[138:139], v[138:139], 0, v[154:155]
	global_store_dwordx4 v[138:139], v[174:177], off sc1
	global_store_dwordx4 v[138:139], v[140:143], off offset:16 sc1
	ds_read2_b32 v[138:139], v173 offset0:96 offset1:112
	s_waitcnt lgkmcnt(0)
	v_mul_f32_e32 v138, 0x3d800000, v138
	v_pk_fma_f32 v[142:143], v[90:91], v[138:139], v[134:135] op_sel_hi:[1,0,1]
	v_pk_fma_f32 v[140:141], v[92:93], v[138:139], v[136:137] op_sel_hi:[1,0,1]
	v_min_f32_e32 v144, 0, v142
	v_mul_f32_e64 v142, |v142|, s33
	v_exp_f32_e32 v142, v142
	v_min_f32_e32 v145, 0, v143
	v_add_f32_e32 v142, 1.0, v142
	v_log_f32_e32 v161, v142
	v_mul_f32_e64 v142, |v143|, s33
	v_exp_f32_e32 v142, v142
	v_min_f32_e32 v143, 0, v141
	v_mul_f32_e64 v141, |v141|, s33
	v_exp_f32_e32 v141, v141
	v_add_f32_e32 v142, 1.0, v142
	v_log_f32_e32 v162, v142
	v_min_f32_e32 v142, 0, v140
	v_mul_f32_e64 v140, |v140|, s33
	v_exp_f32_e32 v140, v140
	v_add_f32_e32 v141, 1.0, v141
	v_log_f32_e32 v141, v141
	v_add_f32_e32 v140, 1.0, v140
	v_log_f32_e32 v140, v140
	v_xor_b32_e32 v141, 0x80000000, v141
	v_xor_b32_e32 v140, 0x80000000, v140
	v_pk_fma_f32 v[142:143], v[140:141], s[46:47], v[142:143] op_sel_hi:[1,0,1]
	v_xor_b32_e32 v141, 0x80000000, v162
	v_xor_b32_e32 v140, 0x80000000, v161
	v_pk_fma_f32 v[140:141], v[140:141], s[46:47], v[144:145] op_sel_hi:[1,0,1]
	v_pk_fma_f32 v[144:145], v[96:97], v[138:139], v[132:133] op_sel_hi:[1,0,1]
	v_pk_fma_f32 v[162:163], v[94:95], v[138:139], v[130:131] op_sel_hi:[1,0,1]
	s_nop 0
	v_min_f32_e32 v174, 0, v162
	v_mul_f32_e64 v138, |v162|, s33
	v_min_f32_e32 v175, 0, v163
	v_mul_f32_e64 v161, |v163|, s33
	v_min_f32_e32 v162, 0, v144
	v_mul_f32_e64 v144, |v144|, s33
	v_min_f32_e32 v163, 0, v145
	v_mul_f32_e64 v145, |v145|, s33
	v_exp_f32_e32 v144, v144
	v_exp_f32_e32 v145, v145
	v_exp_f32_e32 v138, v138
	v_exp_f32_e32 v161, v161
	v_add_f32_e32 v144, 1.0, v144
	v_add_f32_e32 v145, 1.0, v145
	v_add_f32_e32 v138, 1.0, v138
	v_add_f32_e32 v161, 1.0, v161
	v_log_f32_e32 v144, v144
	v_log_f32_e32 v145, v145
	v_log_f32_e32 v138, v138
	v_log_f32_e32 v161, v161
	v_xor_b32_e32 v144, 0x80000000, v144
	v_xor_b32_e32 v145, 0x80000000, v145
	v_pk_fma_f32 v[176:177], v[144:145], s[46:47], v[162:163] op_sel_hi:[1,0,1]
	v_xor_b32_e32 v145, 0x80000000, v161
	v_xor_b32_e32 v144, 0x80000000, v138
	v_pk_fma_f32 v[174:175], v[144:145], s[46:47], v[174:175] op_sel_hi:[1,0,1]
	v_add_u32_e32 v144, 32, v160
	v_ashrrev_i32_e32 v145, 31, v144
	v_lshlrev_b64 v[144:145], 6, v[144:145]
	v_lshl_add_u64 v[144:145], s[24:25], 0, v[144:145]
	v_lshl_add_u64 v[144:145], v[144:145], 0, v[154:155]
	global_store_dwordx4 v[144:145], v[174:177], off sc1
	global_store_dwordx4 v[144:145], v[140:143], off offset:16 sc1
	s_nop 1
	v_mul_f32_e32 v142, 0x3d800000, v139
	v_pk_fma_f32 v[140:141], v[74:75], v[142:143], v[134:135] op_sel_hi:[1,0,1]
	v_pk_fma_f32 v[138:139], v[76:77], v[142:143], v[136:137] op_sel_hi:[1,0,1]
	v_min_f32_e32 v144, 0, v140
	v_mul_f32_e64 v140, |v140|, s33
	v_exp_f32_e32 v140, v140
	v_min_f32_e32 v145, 0, v141
	v_add_f32_e32 v140, 1.0, v140
	v_log_f32_e32 v143, v140
	v_mul_f32_e64 v140, |v141|, s33
	v_exp_f32_e32 v140, v140
	v_min_f32_e32 v141, 0, v139
	v_mul_f32_e64 v139, |v139|, s33
	v_exp_f32_e32 v139, v139
	v_add_f32_e32 v140, 1.0, v140
	v_log_f32_e32 v161, v140
	v_min_f32_e32 v140, 0, v138
	v_mul_f32_e64 v138, |v138|, s33
	v_exp_f32_e32 v138, v138
	v_add_f32_e32 v139, 1.0, v139
	v_log_f32_e32 v139, v139
	v_add_f32_e32 v138, 1.0, v138
	v_log_f32_e32 v138, v138
	v_xor_b32_e32 v139, 0x80000000, v139
	v_xor_b32_e32 v138, 0x80000000, v138
	v_pk_fma_f32 v[140:141], v[138:139], s[46:47], v[140:141] op_sel_hi:[1,0,1]
	v_xor_b32_e32 v139, 0x80000000, v161
	v_xor_b32_e32 v138, 0x80000000, v143
	v_pk_fma_f32 v[138:139], v[138:139], s[46:47], v[144:145] op_sel_hi:[1,0,1]
	v_pk_fma_f32 v[144:145], v[80:81], v[142:143], v[132:133] op_sel_hi:[1,0,1]
	v_pk_fma_f32 v[142:143], v[78:79], v[142:143], v[130:131] op_sel_hi:[1,0,1]
	s_nop 0
	v_min_f32_e32 v162, 0, v142
	v_mul_f32_e64 v142, |v142|, s33
	v_exp_f32_e32 v142, v142
	v_min_f32_e32 v163, 0, v143
	v_add_f32_e32 v142, 1.0, v142
	v_log_f32_e32 v161, v142
	v_mul_f32_e64 v142, |v143|, s33
	v_mul_f32_e64 v143, |v144|, s33
	v_exp_f32_e32 v142, v142
	v_exp_f32_e32 v143, v143
	v_add_f32_e32 v142, 1.0, v142
	v_add_f32_e32 v143, 1.0, v143
	v_log_f32_e32 v174, v142
	v_min_f32_e32 v142, 0, v144
	v_log_f32_e32 v144, v143
	v_min_f32_e32 v143, 0, v145
	v_mul_f32_e64 v145, |v145|, s33
	v_exp_f32_e32 v145, v145
	v_xor_b32_e32 v144, 0x80000000, v144
	v_add_f32_e32 v145, 1.0, v145
	v_log_f32_e32 v145, v145
	s_nop 0
	v_xor_b32_e32 v145, 0x80000000, v145
	v_pk_fma_f32 v[144:145], v[144:145], s[46:47], v[142:143] op_sel_hi:[1,0,1]
	v_xor_b32_e32 v143, 0x80000000, v174
	v_xor_b32_e32 v142, 0x80000000, v161
	v_pk_fma_f32 v[142:143], v[142:143], s[46:47], v[162:163] op_sel_hi:[1,0,1]
	v_add_u32_e32 v162, 48, v160
	v_ashrrev_i32_e32 v163, 31, v162
	v_lshlrev_b64 v[162:163], 6, v[162:163]
	v_lshl_add_u64 v[162:163], s[24:25], 0, v[162:163]
	v_lshl_add_u64 v[162:163], v[162:163], 0, v[154:155]
	global_store_dwordx4 v[162:163], v[142:145], off sc1
	global_store_dwordx4 v[162:163], v[138:141], off offset:16 sc1
	ds_read2_b32 v[138:139], v173 offset0:128 offset1:144
	s_waitcnt lgkmcnt(0)
	v_mul_f32_e32 v138, 0x3d800000, v138
	v_pk_fma_f32 v[142:143], v[58:59], v[138:139], v[134:135] op_sel_hi:[1,0,1]
	v_pk_fma_f32 v[140:141], v[60:61], v[138:139], v[136:137] op_sel_hi:[1,0,1]
	v_min_f32_e32 v144, 0, v142
	v_mul_f32_e64 v142, |v142|, s33
	v_exp_f32_e32 v142, v142
	v_min_f32_e32 v145, 0, v143
	v_add_f32_e32 v142, 1.0, v142
	v_log_f32_e32 v161, v142
	v_mul_f32_e64 v142, |v143|, s33
	v_exp_f32_e32 v142, v142
	v_min_f32_e32 v143, 0, v141
	v_mul_f32_e64 v141, |v141|, s33
	v_exp_f32_e32 v141, v141
	v_add_f32_e32 v142, 1.0, v142
	v_log_f32_e32 v162, v142
	v_min_f32_e32 v142, 0, v140
	v_mul_f32_e64 v140, |v140|, s33
	v_exp_f32_e32 v140, v140
	v_add_f32_e32 v141, 1.0, v141
	v_log_f32_e32 v141, v141
	v_add_f32_e32 v140, 1.0, v140
	v_log_f32_e32 v140, v140
	v_xor_b32_e32 v141, 0x80000000, v141
	v_xor_b32_e32 v140, 0x80000000, v140
	v_pk_fma_f32 v[142:143], v[140:141], s[46:47], v[142:143] op_sel_hi:[1,0,1]
	v_xor_b32_e32 v141, 0x80000000, v162
	v_xor_b32_e32 v140, 0x80000000, v161
	v_pk_fma_f32 v[140:141], v[140:141], s[46:47], v[144:145] op_sel_hi:[1,0,1]
	v_pk_fma_f32 v[144:145], v[64:65], v[138:139], v[132:133] op_sel_hi:[1,0,1]
	v_pk_fma_f32 v[162:163], v[62:63], v[138:139], v[130:131] op_sel_hi:[1,0,1]
	s_nop 0
	v_min_f32_e32 v174, 0, v162
	v_mul_f32_e64 v138, |v162|, s33
	v_min_f32_e32 v175, 0, v163
	v_mul_f32_e64 v161, |v163|, s33
	v_min_f32_e32 v162, 0, v144
	v_mul_f32_e64 v144, |v144|, s33
	v_min_f32_e32 v163, 0, v145
	v_mul_f32_e64 v145, |v145|, s33
	v_exp_f32_e32 v144, v144
	v_exp_f32_e32 v145, v145
	v_exp_f32_e32 v138, v138
	v_exp_f32_e32 v161, v161
	v_add_f32_e32 v144, 1.0, v144
	v_add_f32_e32 v145, 1.0, v145
	v_add_f32_e32 v138, 1.0, v138
	v_add_f32_e32 v161, 1.0, v161
	v_log_f32_e32 v144, v144
	v_log_f32_e32 v145, v145
	v_log_f32_e32 v138, v138
	v_log_f32_e32 v161, v161
	v_xor_b32_e32 v144, 0x80000000, v144
	v_xor_b32_e32 v145, 0x80000000, v145
	v_pk_fma_f32 v[176:177], v[144:145], s[46:47], v[162:163] op_sel_hi:[1,0,1]
	v_xor_b32_e32 v145, 0x80000000, v161
	v_xor_b32_e32 v144, 0x80000000, v138
	v_or_b32_e32 v138, s14, v172
	v_pk_fma_f32 v[174:175], v[144:145], s[46:47], v[174:175] op_sel_hi:[1,0,1]
	v_add_u32_e32 v144, s13, v138
	v_ashrrev_i32_e32 v145, 31, v144
	v_lshlrev_b64 v[144:145], 6, v[144:145]
	v_lshl_add_u64 v[144:145], s[24:25], 0, v[144:145]
	v_lshl_add_u64 v[144:145], v[144:145], 0, v[154:155]
	global_store_dwordx4 v[144:145], v[174:177], off sc1
	global_store_dwordx4 v[144:145], v[140:143], off offset:16 sc1
	s_nop 1
	v_mul_f32_e32 v142, 0x3d800000, v139
	v_pk_fma_f32 v[140:141], v[42:43], v[142:143], v[134:135] op_sel_hi:[1,0,1]
	v_pk_fma_f32 v[138:139], v[44:45], v[142:143], v[136:137] op_sel_hi:[1,0,1]
	v_min_f32_e32 v144, 0, v140
	v_mul_f32_e64 v140, |v140|, s33
	v_exp_f32_e32 v140, v140
	v_min_f32_e32 v145, 0, v141
	v_add_f32_e32 v140, 1.0, v140
	v_log_f32_e32 v143, v140
	v_mul_f32_e64 v140, |v141|, s33
	v_exp_f32_e32 v140, v140
	v_min_f32_e32 v141, 0, v139
	v_mul_f32_e64 v139, |v139|, s33
	v_exp_f32_e32 v139, v139
	v_add_f32_e32 v140, 1.0, v140
	v_log_f32_e32 v161, v140
	v_min_f32_e32 v140, 0, v138
	v_mul_f32_e64 v138, |v138|, s33
	v_exp_f32_e32 v138, v138
	v_add_f32_e32 v139, 1.0, v139
	v_log_f32_e32 v139, v139
	v_add_f32_e32 v138, 1.0, v138
	v_log_f32_e32 v138, v138
	v_xor_b32_e32 v139, 0x80000000, v139
	v_xor_b32_e32 v138, 0x80000000, v138
	v_pk_fma_f32 v[140:141], v[138:139], s[46:47], v[140:141] op_sel_hi:[1,0,1]
	v_xor_b32_e32 v139, 0x80000000, v161
	v_xor_b32_e32 v138, 0x80000000, v143
	v_pk_fma_f32 v[138:139], v[138:139], s[46:47], v[144:145] op_sel_hi:[1,0,1]
	v_pk_fma_f32 v[144:145], v[48:49], v[142:143], v[132:133] op_sel_hi:[1,0,1]
	v_pk_fma_f32 v[142:143], v[46:47], v[142:143], v[130:131] op_sel_hi:[1,0,1]
	s_nop 0
	v_min_f32_e32 v162, 0, v142
	v_mul_f32_e64 v142, |v142|, s33
	v_exp_f32_e32 v142, v142
	v_min_f32_e32 v163, 0, v143
	v_add_f32_e32 v142, 1.0, v142
	v_log_f32_e32 v161, v142
	v_mul_f32_e64 v142, |v143|, s33
	v_mul_f32_e64 v143, |v144|, s33
	v_exp_f32_e32 v142, v142
	v_exp_f32_e32 v143, v143
	v_add_f32_e32 v142, 1.0, v142
	v_add_f32_e32 v143, 1.0, v143
	v_log_f32_e32 v174, v142
	v_min_f32_e32 v142, 0, v144
	v_log_f32_e32 v144, v143
	v_min_f32_e32 v143, 0, v145
	v_mul_f32_e64 v145, |v145|, s33
	v_exp_f32_e32 v145, v145
	v_xor_b32_e32 v144, 0x80000000, v144
	v_add_f32_e32 v145, 1.0, v145
	v_log_f32_e32 v145, v145
	s_nop 0
	v_xor_b32_e32 v145, 0x80000000, v145
	v_pk_fma_f32 v[144:145], v[144:145], s[46:47], v[142:143] op_sel_hi:[1,0,1]
	v_xor_b32_e32 v143, 0x80000000, v174
	v_xor_b32_e32 v142, 0x80000000, v161
	v_pk_fma_f32 v[142:143], v[142:143], s[46:47], v[162:163] op_sel_hi:[1,0,1]
	v_add_u32_e32 v162, 0x90, v160
	v_ashrrev_i32_e32 v163, 31, v162
	v_lshlrev_b64 v[162:163], 6, v[162:163]
	v_lshl_add_u64 v[162:163], s[24:25], 0, v[162:163]
	v_lshl_add_u64 v[162:163], v[162:163], 0, v[154:155]
	global_store_dwordx4 v[162:163], v[142:145], off sc1
	global_store_dwordx4 v[162:163], v[138:141], off offset:16 sc1
	ds_read2_b32 v[138:139], v173 offset0:160 offset1:176
	s_waitcnt lgkmcnt(0)
	v_mul_f32_e32 v138, 0x3d800000, v138
	v_pk_fma_f32 v[142:143], v[26:27], v[138:139], v[134:135] op_sel_hi:[1,0,1]
	v_pk_fma_f32 v[140:141], v[28:29], v[138:139], v[136:137] op_sel_hi:[1,0,1]
	v_min_f32_e32 v144, 0, v142
	v_mul_f32_e64 v142, |v142|, s33
	v_exp_f32_e32 v142, v142
	v_min_f32_e32 v145, 0, v143
	v_add_f32_e32 v142, 1.0, v142
	v_log_f32_e32 v161, v142
	v_mul_f32_e64 v142, |v143|, s33
	v_exp_f32_e32 v142, v142
	v_min_f32_e32 v143, 0, v141
	v_mul_f32_e64 v141, |v141|, s33
	v_exp_f32_e32 v141, v141
	v_add_f32_e32 v142, 1.0, v142
	v_log_f32_e32 v162, v142
	v_min_f32_e32 v142, 0, v140
	v_mul_f32_e64 v140, |v140|, s33
	v_exp_f32_e32 v140, v140
	v_add_f32_e32 v141, 1.0, v141
	v_log_f32_e32 v141, v141
	v_add_f32_e32 v140, 1.0, v140
	v_log_f32_e32 v140, v140
	v_xor_b32_e32 v141, 0x80000000, v141
	v_xor_b32_e32 v140, 0x80000000, v140
	v_pk_fma_f32 v[142:143], v[140:141], s[46:47], v[142:143] op_sel_hi:[1,0,1]
	v_xor_b32_e32 v141, 0x80000000, v162
	v_xor_b32_e32 v140, 0x80000000, v161
	v_pk_fma_f32 v[140:141], v[140:141], s[46:47], v[144:145] op_sel_hi:[1,0,1]
	v_pk_fma_f32 v[144:145], v[32:33], v[138:139], v[132:133] op_sel_hi:[1,0,1]
	v_pk_fma_f32 v[162:163], v[30:31], v[138:139], v[130:131] op_sel_hi:[1,0,1]
	s_nop 0
	v_min_f32_e32 v174, 0, v162
	v_mul_f32_e64 v138, |v162|, s33
	v_min_f32_e32 v175, 0, v163
	v_mul_f32_e64 v161, |v163|, s33
	v_min_f32_e32 v162, 0, v144
	v_mul_f32_e64 v144, |v144|, s33
	v_min_f32_e32 v163, 0, v145
	v_mul_f32_e64 v145, |v145|, s33
	v_exp_f32_e32 v144, v144
	v_exp_f32_e32 v145, v145
	v_exp_f32_e32 v138, v138
	v_exp_f32_e32 v161, v161
	v_add_f32_e32 v144, 1.0, v144
	v_add_f32_e32 v145, 1.0, v145
	v_add_f32_e32 v138, 1.0, v138
	v_add_f32_e32 v161, 1.0, v161
	v_log_f32_e32 v144, v144
	v_log_f32_e32 v145, v145
	v_log_f32_e32 v138, v138
	v_log_f32_e32 v161, v161
	v_xor_b32_e32 v144, 0x80000000, v144
	v_xor_b32_e32 v145, 0x80000000, v145
	v_pk_fma_f32 v[176:177], v[144:145], s[46:47], v[162:163] op_sel_hi:[1,0,1]
	v_xor_b32_e32 v145, 0x80000000, v161
	v_xor_b32_e32 v144, 0x80000000, v138
	v_pk_fma_f32 v[174:175], v[144:145], s[46:47], v[174:175] op_sel_hi:[1,0,1]
	v_add_u32_e32 v144, 0xa0, v160
	v_ashrrev_i32_e32 v145, 31, v144
	v_lshlrev_b64 v[144:145], 6, v[144:145]
	v_lshl_add_u64 v[144:145], s[24:25], 0, v[144:145]
	v_mul_f32_e32 v138, 0x3d800000, v139
	v_lshl_add_u64 v[144:145], v[144:145], 0, v[154:155]
	v_pk_fma_f32 v[134:135], v[10:11], v[138:139], v[134:135] op_sel_hi:[1,0,1]
	global_store_dwordx4 v[144:145], v[174:177], off sc1
	global_store_dwordx4 v[144:145], v[140:143], off offset:16 sc1
	v_pk_fma_f32 v[136:137], v[12:13], v[138:139], v[136:137] op_sel_hi:[1,0,1]
	s_nop 0
	v_min_f32_e32 v140, 0, v134
	v_mul_f32_e64 v134, |v134|, s33
	v_exp_f32_e32 v134, v134
	v_min_f32_e32 v141, 0, v135
	v_add_f32_e32 v134, 1.0, v134
	v_log_f32_e32 v139, v134
	v_mul_f32_e64 v134, |v135|, s33
	v_mul_f32_e64 v135, |v136|, s33
	v_exp_f32_e32 v134, v134
	v_exp_f32_e32 v135, v135
	v_pk_fma_f32 v[130:131], v[14:15], v[138:139], v[130:131] op_sel_hi:[1,0,1]
	v_pk_fma_f32 v[132:133], v[16:17], v[138:139], v[132:133] op_sel_hi:[1,0,1]
	v_add_f32_e32 v134, 1.0, v134
	v_add_f32_e32 v135, 1.0, v135
	v_log_f32_e32 v142, v134
	v_min_f32_e32 v134, 0, v136
	v_log_f32_e32 v136, v135
	v_min_f32_e32 v135, 0, v137
	v_mul_f32_e64 v137, |v137|, s33
	v_exp_f32_e32 v137, v137
	v_min_f32_e32 v138, 0, v130
	v_mul_f32_e64 v130, |v130|, s33
	v_exp_f32_e32 v130, v130
	v_add_f32_e32 v137, 1.0, v137
	v_log_f32_e32 v137, v137
	v_xor_b32_e32 v136, 0x80000000, v136
	v_add_f32_e32 v130, 1.0, v130
	v_xor_b32_e32 v137, 0x80000000, v137
	v_pk_fma_f32 v[136:137], v[136:137], s[46:47], v[134:135] op_sel_hi:[1,0,1]
	v_xor_b32_e32 v135, 0x80000000, v142
	v_xor_b32_e32 v134, 0x80000000, v139
	v_pk_fma_f32 v[134:135], v[134:135], s[46:47], v[140:141] op_sel_hi:[1,0,1]
	v_log_f32_e32 v140, v130
	v_min_f32_e32 v139, 0, v131
	v_mul_f32_e64 v130, |v131|, s33
	v_mul_f32_e64 v131, |v132|, s33
	v_exp_f32_e32 v130, v130
	v_exp_f32_e32 v131, v131
	v_add_f32_e32 v130, 1.0, v130
	v_add_f32_e32 v131, 1.0, v131
	v_log_f32_e32 v141, v130
	v_min_f32_e32 v130, 0, v132
	v_log_f32_e32 v132, v131
	v_min_f32_e32 v131, 0, v133
	v_mul_f32_e64 v133, |v133|, s33
	v_exp_f32_e32 v133, v133
	v_xor_b32_e32 v132, 0x80000000, v132
	v_add_f32_e32 v133, 1.0, v133
	v_log_f32_e32 v133, v133
	s_nop 0
	v_xor_b32_e32 v133, 0x80000000, v133
	v_pk_fma_f32 v[132:133], v[132:133], s[46:47], v[130:131] op_sel_hi:[1,0,1]
	v_xor_b32_e32 v131, 0x80000000, v141
	v_xor_b32_e32 v130, 0x80000000, v140
	v_pk_fma_f32 v[130:131], v[130:131], s[46:47], v[138:139] op_sel_hi:[1,0,1]
	v_add_u32_e32 v138, 0xb0, v160
	v_ashrrev_i32_e32 v139, 31, v138
	v_lshlrev_b64 v[138:139], 6, v[138:139]
	v_lshl_add_u64 v[138:139], s[24:25], 0, v[138:139]
	v_lshl_add_u64 v[138:139], v[138:139], 0, v[154:155]
	global_store_dwordx4 v[138:139], v[130:133], off sc1
	global_store_dwordx4 v[138:139], v[134:137], off offset:16 sc1

.LBB0_1854:
	s_andn2_b64 vcc, exec, s[10:11]
	s_cbranch_vccnz .LBB0_1937
	s_ashr_i32 s82, s12, 2
	s_ashr_i32 s83, s82, 31
	s_lshl_b64 s[10:11], s[82:83], 27
	s_add_u32 s17, s67, s10
	s_addc_u32 s68, s60, s11
	s_cmp_gt_u32 s12, 3
	v_lshl_add_u32 v174, v172, 2, s19
	s_cselect_b64 s[10:11], -1, 0
	s_cmp_lt_u32 s12, 4
	ds_read_b32 v130, v174 offset:2304
	s_cselect_b64 vcc, -1, 0
	s_lshl_b32 s13, s12, 2
	s_and_b32 s51, s13, 12
	s_cmp_lg_u32 s82, 1
	v_cndmask_b32_e32 v173, 1.0, v168, vcc
	s_cselect_b64 s[14:15], -1, 0
	s_lshl_b32 s12, s12, 9
	s_lshl_b32 s13, s49, 7
	s_and_b32 s12, s12, 0x600
	s_waitcnt lgkmcnt(0)
	v_mul_f32_e32 v130, v173, v130
	s_or_b32 s12, s13, s12
	v_mul_f32_e32 v130, 0x3d800000, v130
	s_add_u32 s77, s17, s12
	v_pk_mul_f32 v[142:143], v[120:121], v[130:131] op_sel_hi:[1,0]
	v_pk_mul_f32 v[160:161], v[118:119], v[130:131] op_sel_hi:[1,0]
	v_mul_u32_u24_e32 v118, 0x90, v172
	v_and_b32_e32 v119, 48, v171
	v_lshrrev_b32_e32 v176, 3, v170
	v_and_b32_e32 v120, 7, v171
	s_addc_u32 s16, s68, 0
	v_pk_mul_f32 v[134:135], v[128:129], v[130:131] op_sel_hi:[1,0]
	v_pk_mul_f32 v[138:139], v[126:127], v[130:131] op_sel_hi:[1,0]
	v_pk_mul_f32 v[132:133], v[124:125], v[130:131] op_sel_hi:[1,0]
	v_pk_mul_f32 v[136:137], v[122:123], v[130:131] op_sel_hi:[1,0]
	v_pk_mul_f32 v[140:141], v[116:117], v[130:131] op_sel_hi:[1,0]
	v_pk_mul_f32 v[144:145], v[114:115], v[130:131] op_sel_hi:[1,0]
	s_mov_b64 s[12:13], -1
	s_and_b64 vcc, exec, s[10:11]
	v_add3_u32 v162, s19, v118, v119
	v_mul_u32_u24_e32 v163, 0x90, v176
	v_lshlrev_b32_e32 v171, 4, v120
	v_lshlrev_b32_e32 v130, 10, v120
	v_cvt_pk_bf16_f32 v122, v138, v139
	v_cvt_pk_bf16_f32 v123, v134, v135
	v_cvt_pk_bf16_f32 v124, v136, v137
	v_cvt_pk_bf16_f32 v125, v132, v133
	v_cvt_pk_bf16_f32 v114, v160, v161
	v_cvt_pk_bf16_f32 v115, v142, v143
	v_cvt_pk_bf16_f32 v116, v144, v145
	v_cvt_pk_bf16_f32 v117, v140, v141
	s_cbranch_vccz .LBB0_1861
	s_ashr_i32 s12, s78, 9
	s_and_b32 s12, s12, -16
	s_or_b32 s12, s51, s12
	s_or_b32 s12, s12, s49
	ds_write_b128 v162, v[122:125]
	ds_write_b128 v162, v[114:117] offset:64
	v_add3_u32 v126, s19, v163, v171
	s_ashr_i32 s13, s12, 31
	s_lshl_b32 s79, s78, 7
	ds_read_b128 v[118:121], v126
	ds_read_b128 v[126:129], v126 offset:1152
	s_lshl_b64 s[12:13], s[12:13], 20
	s_and_b32 s79, s79, 0xfe000
	s_add_u32 s12, s17, s12
	s_addc_u32 s13, s68, s13
	s_add_u32 s12, s12, s79
	s_addc_u32 s13, s13, 0
	s_mov_b64 s[84:85], -1
	s_and_b64 vcc, exec, s[14:15]
	s_cbranch_vccz .LBB0_1858
	v_and_b32_e32 v154, 0x1000, v130
	v_lshl_add_u64 v[178:179], s[12:13], 0, v[154:155]
	v_lshlrev_b32_e32 v154, 6, v176
	v_lshlrev_b32_e32 v131, 4, v170
	v_lshl_add_u64 v[178:179], v[178:179], 0, v[154:155]
	v_and_b32_e32 v154, 48, v131
	v_lshl_add_u64 v[178:179], v[178:179], 0, v[154:155]
	s_waitcnt lgkmcnt(1)
	global_store_dwordx4 v[178:179], v[118:121], off sc1
	s_waitcnt lgkmcnt(0)
	global_store_dwordx4 v[178:179], v[126:129], off offset:512 sc1
	s_mov_b64 s[84:85], 0
.LBB0_1858:
	s_andn2_b64 vcc, exec, s[84:85]
	s_cbranch_vccnz .LBB0_1860
	v_mov_b32_e32 v131, v155
	v_lshl_add_u64 v[178:179], s[12:13], 0, v[130:131]
	v_lshlrev_b32_e32 v154, 4, v176
	v_lshl_add_u64 v[178:179], v[178:179], 0, v[154:155]
	s_waitcnt lgkmcnt(1)
	global_store_dwordx4 v[178:179], v[118:121], off sc1
	s_waitcnt lgkmcnt(0)
	global_store_dwordx4 v[178:179], v[126:129], off offset:128 sc1

.LBB0_1861:
	v_lshlrev_b32_e32 v175, 4, v170
	s_andn2_b64 vcc, exec, s[12:13]
	s_waitcnt lgkmcnt(1)
	v_and_b32_e32 v118, 0x70, v175
	v_lshlrev_b32_e32 v154, 11, v176
	s_cbranch_vccnz .LBB0_1863
	s_ashr_i32 s79, s78, 31
	s_lshl_b64 s[12:13], s[78:79], 11
	ds_write_b128 v162, v[122:125]
	ds_write_b128 v162, v[114:117] offset:64
	v_add3_u32 v119, s19, v163, v118
	s_add_u32 s12, s77, s12
	ds_read_b128 v[114:117], v119
	ds_read_b128 v[120:123], v119 offset:1152
	s_addc_u32 s13, s16, s13
	v_lshl_add_u64 v[124:125], s[12:13], 0, v[154:155]
	v_mov_b32_e32 v119, v155
	v_lshl_add_u64 v[124:125], v[124:125], 0, v[118:119]
	s_waitcnt lgkmcnt(1)
	global_store_dwordx4 v[124:125], v[114:117], off sc1
	s_nop 1
	v_or_b32_e32 v114, 0x4000, v154
	v_mov_b32_e32 v115, v155
	v_lshl_add_u64 v[114:115], s[12:13], 0, v[114:115]
	v_lshl_add_u64 v[114:115], v[114:115], 0, v[118:119]
	s_waitcnt lgkmcnt(0)
	global_store_dwordx4 v[114:115], v[120:123], off sc1

.LBB0_1865:
	ds_read_b32 v114, v174 offset:2368
	s_mov_b64 s[86:87], -1
	s_andn2_b64 vcc, exec, s[10:11]
	v_or_b32_e32 v134, 16, v176
	s_waitcnt lgkmcnt(0)
	v_mul_f32_e32 v114, v173, v114
	v_mul_f32_e32 v128, 0x3d800000, v114
	v_pk_mul_f32 v[132:133], v[102:103], v[128:129] op_sel_hi:[1,0]
	v_cndmask_b32_e64 v102, 0, 1, s[10:11]
	v_cmp_ne_u32_e64 s[12:13], 1, v102
	v_cndmask_b32_e64 v102, 0, 1, s[14:15]
	v_pk_mul_f32 v[116:117], v[112:113], v[128:129] op_sel_hi:[1,0]
	v_pk_mul_f32 v[124:125], v[110:111], v[128:129] op_sel_hi:[1,0]
	v_pk_mul_f32 v[114:115], v[108:109], v[128:129] op_sel_hi:[1,0]
	v_pk_mul_f32 v[120:121], v[106:107], v[128:129] op_sel_hi:[1,0]
	v_pk_mul_f32 v[126:127], v[104:105], v[128:129] op_sel_hi:[1,0]
	v_pk_mul_f32 v[122:123], v[100:101], v[128:129] op_sel_hi:[1,0]
	v_pk_mul_f32 v[128:129], v[98:99], v[128:129] op_sel_hi:[1,0]
	v_cmp_ne_u32_e64 s[10:11], 1, v102
	v_cvt_pk_bf16_f32 v106, v124, v125
	v_cvt_pk_bf16_f32 v107, v116, v117
	v_cvt_pk_bf16_f32 v108, v120, v121
	v_cvt_pk_bf16_f32 v109, v114, v115
	v_cvt_pk_bf16_f32 v98, v132, v133
	v_cvt_pk_bf16_f32 v99, v126, v127
	v_cvt_pk_bf16_f32 v100, v128, v129
	v_cvt_pk_bf16_f32 v101, v122, v123
	s_cbranch_vccnz .LBB0_1923
	s_ashr_i32 s14, s78, 9
	s_and_b32 s14, s14, -16
	s_or_b32 s14, s51, s14
	s_or_b32 s14, s14, s49
	ds_write_b128 v162, v[106:109]
	ds_write_b128 v162, v[98:101] offset:64
	v_add3_u32 v110, s19, v163, v171
	s_ashr_i32 s15, s14, 31
	s_lshl_b32 s79, s78, 7
	ds_read_b128 v[102:105], v110
	ds_read_b128 v[110:113], v110 offset:1152
	s_lshl_b64 s[14:15], s[14:15], 20
	s_and_b32 s79, s79, 0xfe000
	s_add_u32 s14, s17, s14
	s_addc_u32 s15, s68, s15
	s_add_u32 s14, s14, s79
	s_addc_u32 s15, s15, 0
	s_and_b64 vcc, exec, s[10:11]
	s_cbranch_vccnz .LBB0_1868
	v_and_b32_e32 v136, 0x1000, v130
	v_mov_b32_e32 v137, v155
	v_lshl_add_u64 v[136:137], s[14:15], 0, v[136:137]
	v_lshlrev_b32_e32 v138, 6, v134
	v_mov_b32_e32 v139, v155
	v_lshl_add_u64 v[136:137], v[136:137], 0, v[138:139]
	v_and_b32_e32 v138, 48, v175
	v_lshl_add_u64 v[136:137], v[136:137], 0, v[138:139]
	s_mov_b64 s[86:87], 0
	s_waitcnt lgkmcnt(1)
	global_store_dwordx4 v[136:137], v[102:105], off sc1
	s_waitcnt lgkmcnt(0)
	global_store_dwordx4 v[136:137], v[110:113], off offset:512 sc1
.LBB0_1868:
	s_andn2_b64 vcc, exec, s[86:87]
	s_cbranch_vccnz .LBB0_1870
	v_mov_b32_e32 v131, v155
	v_lshl_add_u64 v[136:137], s[14:15], 0, v[130:131]
	v_lshlrev_b32_e32 v138, 4, v134
	v_mov_b32_e32 v139, v155
	v_lshl_add_u64 v[136:137], v[136:137], 0, v[138:139]
	s_waitcnt lgkmcnt(1)
	global_store_dwordx4 v[136:137], v[102:105], off sc1
	s_waitcnt lgkmcnt(0)
	global_store_dwordx4 v[136:137], v[110:113], off offset:128 sc1

.LBB0_1873:
	ds_read_b32 v98, v174 offset:2432
	s_mov_b64 s[84:85], -1
	s_and_b64 vcc, exec, s[12:13]
	v_or_b32_e32 v114, 32, v176
	s_waitcnt lgkmcnt(0)
	v_mul_f32_e32 v98, v173, v98
	v_mul_f32_e32 v110, 0x3d800000, v98
	v_pk_mul_f32 v[100:101], v[96:97], v[110:111] op_sel_hi:[1,0]
	v_pk_mul_f32 v[106:107], v[94:95], v[110:111] op_sel_hi:[1,0]
	v_pk_mul_f32 v[98:99], v[92:93], v[110:111] op_sel_hi:[1,0]
	v_pk_mul_f32 v[102:103], v[90:91], v[110:111] op_sel_hi:[1,0]
	v_pk_mul_f32 v[108:109], v[88:89], v[110:111] op_sel_hi:[1,0]
	v_pk_mul_f32 v[112:113], v[86:87], v[110:111] op_sel_hi:[1,0]
	v_pk_mul_f32 v[104:105], v[84:85], v[110:111] op_sel_hi:[1,0]
	v_pk_mul_f32 v[110:111], v[82:83], v[110:111] op_sel_hi:[1,0]
	v_cvt_pk_bf16_f32 v90, v106, v107
	v_cvt_pk_bf16_f32 v91, v100, v101
	v_cvt_pk_bf16_f32 v92, v102, v103
	v_cvt_pk_bf16_f32 v93, v98, v99
	v_cvt_pk_bf16_f32 v82, v112, v113
	v_cvt_pk_bf16_f32 v83, v108, v109
	s_nop 0
	v_cvt_pk_bf16_f32 v84, v110, v111
	v_cvt_pk_bf16_f32 v85, v104, v105
	s_cbranch_vccnz .LBB0_1925
	s_ashr_i32 s79, s78, 9
	s_and_b32 s79, s79, -16
	s_or_b32 s79, s51, s79
	s_or_b32 s84, s79, s49
	ds_write_b128 v162, v[90:93]
	ds_write_b128 v162, v[82:85] offset:64
	v_add3_u32 v94, s19, v163, v171
	s_ashr_i32 s85, s84, 31
	s_lshl_b32 s79, s78, 7
	ds_read_b128 v[86:89], v94
	ds_read_b128 v[94:97], v94 offset:1152
	s_lshl_b64 s[84:85], s[84:85], 20
	s_and_b32 s79, s79, 0xfe000
	s_add_u32 s81, s17, s84
	s_addc_u32 s85, s68, s85
	s_add_u32 s84, s81, s79
	s_addc_u32 s85, s85, 0
	s_and_b64 vcc, exec, s[10:11]
	s_mov_b64 s[86:87], -1
	s_cbranch_vccnz .LBB0_1876
	v_and_b32_e32 v116, 0x1000, v130
	v_mov_b32_e32 v117, v155
	v_lshl_add_u64 v[116:117], s[84:85], 0, v[116:117]
	v_lshlrev_b32_e32 v120, 6, v114
	v_mov_b32_e32 v121, v155
	v_lshl_add_u64 v[116:117], v[116:117], 0, v[120:121]
	v_and_b32_e32 v120, 48, v175
	v_lshl_add_u64 v[116:117], v[116:117], 0, v[120:121]
	s_mov_b64 s[86:87], 0
	s_waitcnt lgkmcnt(1)
	global_store_dwordx4 v[116:117], v[86:89], off sc1
	s_waitcnt lgkmcnt(0)
	global_store_dwordx4 v[116:117], v[94:97], off offset:512 sc1
.LBB0_1876:
	s_andn2_b64 vcc, exec, s[86:87]
	s_cbranch_vccnz .LBB0_1878
	v_mov_b32_e32 v131, v155
	v_lshl_add_u64 v[116:117], s[84:85], 0, v[130:131]
	v_lshlrev_b32_e32 v120, 4, v114
	v_mov_b32_e32 v121, v155
	v_lshl_add_u64 v[116:117], v[116:117], 0, v[120:121]
	s_waitcnt lgkmcnt(1)
	global_store_dwordx4 v[116:117], v[86:89], off sc1
	s_waitcnt lgkmcnt(0)
	global_store_dwordx4 v[116:117], v[94:97], off offset:128 sc1

.LBB0_1881:
	ds_read_b32 v82, v174 offset:2496
	s_mov_b64 s[84:85], -1
	s_and_b64 vcc, exec, s[12:13]
	v_or_b32_e32 v98, 48, v176
	s_waitcnt lgkmcnt(0)
	v_mul_f32_e32 v82, v173, v82
	v_mul_f32_e32 v94, 0x3d800000, v82
	v_pk_mul_f32 v[84:85], v[80:81], v[94:95] op_sel_hi:[1,0]
	v_pk_mul_f32 v[90:91], v[78:79], v[94:95] op_sel_hi:[1,0]
	v_pk_mul_f32 v[82:83], v[76:77], v[94:95] op_sel_hi:[1,0]
	v_pk_mul_f32 v[86:87], v[74:75], v[94:95] op_sel_hi:[1,0]
	v_pk_mul_f32 v[92:93], v[72:73], v[94:95] op_sel_hi:[1,0]
	v_pk_mul_f32 v[96:97], v[70:71], v[94:95] op_sel_hi:[1,0]
	v_pk_mul_f32 v[88:89], v[68:69], v[94:95] op_sel_hi:[1,0]
	v_pk_mul_f32 v[94:95], v[66:67], v[94:95] op_sel_hi:[1,0]
	v_cvt_pk_bf16_f32 v74, v90, v91
	v_cvt_pk_bf16_f32 v75, v84, v85
	v_cvt_pk_bf16_f32 v76, v86, v87
	v_cvt_pk_bf16_f32 v77, v82, v83
	v_cvt_pk_bf16_f32 v66, v96, v97
	v_cvt_pk_bf16_f32 v67, v92, v93
	s_nop 0
	v_cvt_pk_bf16_f32 v68, v94, v95
	v_cvt_pk_bf16_f32 v69, v88, v89
	s_cbranch_vccnz .LBB0_1927
	s_ashr_i32 s79, s78, 9
	s_and_b32 s79, s79, -16
	s_or_b32 s79, s51, s79
	s_or_b32 s84, s79, s49
	ds_write_b128 v162, v[74:77]
	ds_write_b128 v162, v[66:69] offset:64
	v_add3_u32 v78, s19, v163, v171
	s_ashr_i32 s85, s84, 31
	s_lshl_b32 s79, s78, 7
	ds_read_b128 v[70:73], v78
	ds_read_b128 v[78:81], v78 offset:1152
	s_lshl_b64 s[84:85], s[84:85], 20
	s_and_b32 s79, s79, 0xfe000
	s_add_u32 s81, s17, s84
	s_addc_u32 s85, s68, s85
	s_add_u32 s84, s81, s79
	s_addc_u32 s85, s85, 0
	s_and_b64 vcc, exec, s[10:11]
	s_mov_b64 s[86:87], -1
	s_cbranch_vccnz .LBB0_1884
	v_and_b32_e32 v100, 0x1000, v130
	v_mov_b32_e32 v101, v155
	v_lshl_add_u64 v[100:101], s[84:85], 0, v[100:101]
	v_lshlrev_b32_e32 v102, 6, v98
	v_mov_b32_e32 v103, v155
	v_lshl_add_u64 v[100:101], v[100:101], 0, v[102:103]
	v_and_b32_e32 v102, 48, v175
	v_lshl_add_u64 v[100:101], v[100:101], 0, v[102:103]
	s_mov_b64 s[86:87], 0
	s_waitcnt lgkmcnt(1)
	global_store_dwordx4 v[100:101], v[70:73], off sc1
	s_waitcnt lgkmcnt(0)
	global_store_dwordx4 v[100:101], v[78:81], off offset:512 sc1
.LBB0_1884:
	s_andn2_b64 vcc, exec, s[86:87]
	s_cbranch_vccnz .LBB0_1886
	v_mov_b32_e32 v131, v155
	v_lshl_add_u64 v[100:101], s[84:85], 0, v[130:131]
	v_lshlrev_b32_e32 v102, 4, v98
	v_mov_b32_e32 v103, v155
	v_lshl_add_u64 v[100:101], v[100:101], 0, v[102:103]
	s_waitcnt lgkmcnt(1)
	global_store_dwordx4 v[100:101], v[70:73], off sc1
	s_waitcnt lgkmcnt(0)
	global_store_dwordx4 v[100:101], v[78:81], off offset:128 sc1

.LBB0_1889:
	ds_read_b32 v66, v174 offset:2560
	s_and_b64 vcc, exec, s[12:13]
	s_mov_b64 s[84:85], -1
	s_waitcnt lgkmcnt(0)
	v_mul_f32_e32 v66, v173, v66
	v_mul_f32_e32 v78, 0x3d800000, v66
	v_pk_mul_f32 v[68:69], v[64:65], v[78:79] op_sel_hi:[1,0]
	v_pk_mul_f32 v[72:73], v[62:63], v[78:79] op_sel_hi:[1,0]
	v_pk_mul_f32 v[66:67], v[60:61], v[78:79] op_sel_hi:[1,0]
	v_pk_mul_f32 v[70:71], v[58:59], v[78:79] op_sel_hi:[1,0]
	v_pk_mul_f32 v[76:77], v[56:57], v[78:79] op_sel_hi:[1,0]
	v_pk_mul_f32 v[80:81], v[54:55], v[78:79] op_sel_hi:[1,0]
	v_pk_mul_f32 v[74:75], v[52:53], v[78:79] op_sel_hi:[1,0]
	v_pk_mul_f32 v[78:79], v[50:51], v[78:79] op_sel_hi:[1,0]
	v_cvt_pk_bf16_f32 v58, v72, v73
	v_cvt_pk_bf16_f32 v59, v68, v69
	v_cvt_pk_bf16_f32 v60, v70, v71
	v_cvt_pk_bf16_f32 v61, v66, v67
	v_cvt_pk_bf16_f32 v50, v80, v81
	v_cvt_pk_bf16_f32 v51, v76, v77
	s_nop 0
	v_cvt_pk_bf16_f32 v52, v78, v79
	v_cvt_pk_bf16_f32 v53, v74, v75
	s_cbranch_vccnz .LBB0_1929
	s_ashr_i32 s79, s80, 9
	s_and_b32 s79, s79, -16
	s_or_b32 s79, s51, s79
	s_or_b32 s84, s79, s49
	ds_write_b128 v162, v[58:61]
	ds_write_b128 v162, v[50:53] offset:64
	v_add3_u32 v62, s19, v163, v171
	s_ashr_i32 s85, s84, 31
	s_lshl_b32 s79, s80, 7
	ds_read_b128 v[54:57], v62
	ds_read_b128 v[62:65], v62 offset:1152
	s_lshl_b64 s[84:85], s[84:85], 20
	s_and_b32 s79, s79, 0xfe000
	s_add_u32 s81, s17, s84
	s_addc_u32 s85, s68, s85
	s_add_u32 s84, s81, s79
	s_addc_u32 s85, s85, 0
	s_and_b64 vcc, exec, s[10:11]
	s_mov_b64 s[86:87], -1
	s_cbranch_vccnz .LBB0_1892
	v_and_b32_e32 v82, 0x1000, v130
	v_mov_b32_e32 v83, v155
	v_lshl_add_u64 v[82:83], s[84:85], 0, v[82:83]
	v_lshlrev_b32_e32 v84, 6, v176
	v_mov_b32_e32 v85, v155
	v_lshl_add_u64 v[82:83], v[82:83], 0, v[84:85]
	v_and_b32_e32 v84, 48, v175
	v_lshl_add_u64 v[82:83], v[82:83], 0, v[84:85]
	s_mov_b64 s[86:87], 0
	s_waitcnt lgkmcnt(1)
	global_store_dwordx4 v[82:83], v[54:57], off sc1
	s_waitcnt lgkmcnt(0)
	global_store_dwordx4 v[82:83], v[62:65], off offset:512 sc1
.LBB0_1892:
	s_andn2_b64 vcc, exec, s[86:87]
	s_cbranch_vccnz .LBB0_1894
	v_mov_b32_e32 v131, v155
	v_lshl_add_u64 v[82:83], s[84:85], 0, v[130:131]
	v_lshlrev_b32_e32 v84, 4, v176
	v_mov_b32_e32 v85, v155
	v_lshl_add_u64 v[82:83], v[82:83], 0, v[84:85]
	s_waitcnt lgkmcnt(1)
	global_store_dwordx4 v[82:83], v[54:57], off sc1
	s_waitcnt lgkmcnt(0)
	global_store_dwordx4 v[82:83], v[62:65], off offset:128 sc1

.LBB0_1897:
	ds_read_b32 v50, v174 offset:2624
	s_and_b64 vcc, exec, s[12:13]
	s_mov_b64 s[84:85], -1
	s_waitcnt lgkmcnt(0)
	v_mul_f32_e32 v50, v173, v50
	v_mul_f32_e32 v62, 0x3d800000, v50
	v_pk_mul_f32 v[52:53], v[48:49], v[62:63] op_sel_hi:[1,0]
	v_pk_mul_f32 v[58:59], v[46:47], v[62:63] op_sel_hi:[1,0]
	v_pk_mul_f32 v[50:51], v[44:45], v[62:63] op_sel_hi:[1,0]
	v_pk_mul_f32 v[54:55], v[42:43], v[62:63] op_sel_hi:[1,0]
	v_pk_mul_f32 v[60:61], v[40:41], v[62:63] op_sel_hi:[1,0]
	v_pk_mul_f32 v[64:65], v[38:39], v[62:63] op_sel_hi:[1,0]
	v_pk_mul_f32 v[56:57], v[36:37], v[62:63] op_sel_hi:[1,0]
	v_pk_mul_f32 v[62:63], v[34:35], v[62:63] op_sel_hi:[1,0]
	v_cvt_pk_bf16_f32 v42, v58, v59
	v_cvt_pk_bf16_f32 v43, v52, v53
	v_cvt_pk_bf16_f32 v44, v54, v55
	v_cvt_pk_bf16_f32 v45, v50, v51
	v_cvt_pk_bf16_f32 v34, v64, v65
	v_cvt_pk_bf16_f32 v35, v60, v61
	s_nop 0
	v_cvt_pk_bf16_f32 v36, v62, v63
	v_cvt_pk_bf16_f32 v37, v56, v57
	s_cbranch_vccnz .LBB0_1931
	s_ashr_i32 s79, s80, 9
	s_and_b32 s79, s79, -16
	s_or_b32 s79, s51, s79
	s_or_b32 s84, s79, s49
	ds_write_b128 v162, v[42:45]
	ds_write_b128 v162, v[34:37] offset:64
	v_add3_u32 v46, s19, v163, v171
	s_ashr_i32 s85, s84, 31
	s_lshl_b32 s79, s80, 7
	ds_read_b128 v[38:41], v46
	ds_read_b128 v[46:49], v46 offset:1152
	s_lshl_b64 s[84:85], s[84:85], 20
	s_and_b32 s79, s79, 0xfe000
	s_add_u32 s81, s17, s84
	s_addc_u32 s85, s68, s85
	s_add_u32 s84, s81, s79
	s_addc_u32 s85, s85, 0
	s_and_b64 vcc, exec, s[10:11]
	s_mov_b64 s[86:87], -1
	s_cbranch_vccnz .LBB0_1900
	v_and_b32_e32 v66, 0x1000, v130
	v_mov_b32_e32 v67, v155
	v_lshl_add_u64 v[66:67], s[84:85], 0, v[66:67]
	v_lshlrev_b32_e32 v68, 6, v134
	v_mov_b32_e32 v69, v155
	v_lshl_add_u64 v[66:67], v[66:67], 0, v[68:69]
	v_and_b32_e32 v68, 48, v175
	v_lshl_add_u64 v[66:67], v[66:67], 0, v[68:69]
	s_mov_b64 s[86:87], 0
	s_waitcnt lgkmcnt(1)
	global_store_dwordx4 v[66:67], v[38:41], off sc1
	s_waitcnt lgkmcnt(0)
	global_store_dwordx4 v[66:67], v[46:49], off offset:512 sc1
.LBB0_1900:
	s_andn2_b64 vcc, exec, s[86:87]
	s_cbranch_vccnz .LBB0_1902
	v_mov_b32_e32 v131, v155
	v_lshl_add_u64 v[66:67], s[84:85], 0, v[130:131]
	v_lshlrev_b32_e32 v68, 4, v134
	v_mov_b32_e32 v69, v155
	v_lshl_add_u64 v[66:67], v[66:67], 0, v[68:69]
	s_waitcnt lgkmcnt(1)
	global_store_dwordx4 v[66:67], v[38:41], off sc1
	s_waitcnt lgkmcnt(0)
	global_store_dwordx4 v[66:67], v[46:49], off offset:128 sc1

.LBB0_1905:
	ds_read_b32 v34, v174 offset:2688
	s_and_b64 vcc, exec, s[12:13]
	s_mov_b64 s[84:85], -1
	s_waitcnt lgkmcnt(0)
	v_mul_f32_e32 v34, v173, v34
	v_mul_f32_e32 v46, 0x3d800000, v34
	v_pk_mul_f32 v[36:37], v[32:33], v[46:47] op_sel_hi:[1,0]
	v_pk_mul_f32 v[42:43], v[30:31], v[46:47] op_sel_hi:[1,0]
	v_pk_mul_f32 v[34:35], v[28:29], v[46:47] op_sel_hi:[1,0]
	v_pk_mul_f32 v[38:39], v[26:27], v[46:47] op_sel_hi:[1,0]
	v_pk_mul_f32 v[44:45], v[24:25], v[46:47] op_sel_hi:[1,0]
	v_pk_mul_f32 v[48:49], v[22:23], v[46:47] op_sel_hi:[1,0]
	v_pk_mul_f32 v[40:41], v[20:21], v[46:47] op_sel_hi:[1,0]
	v_pk_mul_f32 v[46:47], v[18:19], v[46:47] op_sel_hi:[1,0]
	v_cvt_pk_bf16_f32 v26, v42, v43
	v_cvt_pk_bf16_f32 v27, v36, v37
	v_cvt_pk_bf16_f32 v28, v38, v39
	v_cvt_pk_bf16_f32 v29, v34, v35
	v_cvt_pk_bf16_f32 v18, v48, v49
	v_cvt_pk_bf16_f32 v19, v44, v45
	s_nop 0
	v_cvt_pk_bf16_f32 v20, v46, v47
	v_cvt_pk_bf16_f32 v21, v40, v41
	s_cbranch_vccnz .LBB0_1933
	s_ashr_i32 s79, s80, 9
	s_and_b32 s79, s79, -16
	s_or_b32 s79, s51, s79
	s_or_b32 s84, s79, s49
	ds_write_b128 v162, v[26:29]
	ds_write_b128 v162, v[18:21] offset:64
	v_add3_u32 v30, s19, v163, v171
	s_ashr_i32 s85, s84, 31
	s_lshl_b32 s79, s80, 7
	ds_read_b128 v[22:25], v30
	ds_read_b128 v[30:33], v30 offset:1152
	s_lshl_b64 s[84:85], s[84:85], 20
	s_and_b32 s79, s79, 0xfe000
	s_add_u32 s81, s17, s84
	s_addc_u32 s85, s68, s85
	s_add_u32 s84, s81, s79
	s_addc_u32 s85, s85, 0
	s_and_b64 vcc, exec, s[10:11]
	s_mov_b64 s[86:87], -1
	s_cbranch_vccnz .LBB0_1908
	v_and_b32_e32 v50, 0x1000, v130
	v_mov_b32_e32 v51, v155
	v_lshl_add_u64 v[50:51], s[84:85], 0, v[50:51]
	v_lshlrev_b32_e32 v52, 6, v114
	v_mov_b32_e32 v53, v155
	v_lshl_add_u64 v[50:51], v[50:51], 0, v[52:53]
	v_and_b32_e32 v52, 48, v175
	v_lshl_add_u64 v[50:51], v[50:51], 0, v[52:53]
	s_mov_b64 s[86:87], 0
	s_waitcnt lgkmcnt(1)
	global_store_dwordx4 v[50:51], v[22:25], off sc1
	s_waitcnt lgkmcnt(0)
	global_store_dwordx4 v[50:51], v[30:33], off offset:512 sc1
.LBB0_1908:
	s_andn2_b64 vcc, exec, s[86:87]
	s_cbranch_vccnz .LBB0_1910
	v_mov_b32_e32 v131, v155
	v_lshl_add_u64 v[50:51], s[84:85], 0, v[130:131]
	v_lshlrev_b32_e32 v52, 4, v114
	v_mov_b32_e32 v53, v155
	v_lshl_add_u64 v[50:51], v[50:51], 0, v[52:53]
	s_waitcnt lgkmcnt(1)
	global_store_dwordx4 v[50:51], v[22:25], off sc1
	s_waitcnt lgkmcnt(0)
	global_store_dwordx4 v[50:51], v[30:33], off offset:128 sc1

.LBB0_1913:
	ds_read_b32 v18, v174 offset:2752
	s_and_b64 vcc, exec, s[12:13]
	s_mov_b64 s[12:13], -1
	s_waitcnt lgkmcnt(0)
	v_mul_f32_e32 v18, v173, v18
	v_mul_f32_e32 v30, 0x3d800000, v18
	v_pk_mul_f32 v[20:21], v[16:17], v[30:31] op_sel_hi:[1,0]
	v_pk_mul_f32 v[26:27], v[14:15], v[30:31] op_sel_hi:[1,0]
	v_pk_mul_f32 v[18:19], v[12:13], v[30:31] op_sel_hi:[1,0]
	v_pk_mul_f32 v[22:23], v[10:11], v[30:31] op_sel_hi:[1,0]
	v_pk_mul_f32 v[28:29], v[8:9], v[30:31] op_sel_hi:[1,0]
	v_pk_mul_f32 v[32:33], v[6:7], v[30:31] op_sel_hi:[1,0]
	v_pk_mul_f32 v[24:25], v[4:5], v[30:31] op_sel_hi:[1,0]
	v_pk_mul_f32 v[30:31], v[2:3], v[30:31] op_sel_hi:[1,0]
	v_cvt_pk_bf16_f32 v10, v26, v27
	v_cvt_pk_bf16_f32 v11, v20, v21
	v_cvt_pk_bf16_f32 v12, v22, v23
	v_cvt_pk_bf16_f32 v13, v18, v19
	v_cvt_pk_bf16_f32 v2, v32, v33
	v_cvt_pk_bf16_f32 v3, v28, v29
	s_nop 0
	v_cvt_pk_bf16_f32 v4, v30, v31
	v_cvt_pk_bf16_f32 v5, v24, v25
	s_cbranch_vccnz .LBB0_1935
	s_ashr_i32 s12, s80, 9
	s_and_b32 s12, s12, -16
	s_or_b32 s12, s51, s12
	s_or_b32 s12, s12, s49
	ds_write_b128 v162, v[10:13]
	ds_write_b128 v162, v[2:5] offset:64
	v_add3_u32 v14, s19, v163, v171
	s_ashr_i32 s13, s12, 31
	s_lshl_b32 s79, s80, 7
	ds_read_b128 v[6:9], v14
	ds_read_b128 v[14:17], v14 offset:1152
	s_lshl_b64 s[12:13], s[12:13], 20
	s_and_b32 s79, s79, 0xfe000
	s_add_u32 s12, s17, s12
	s_addc_u32 s13, s68, s13
	s_add_u32 s12, s12, s79
	s_addc_u32 s13, s13, 0
	s_and_b64 vcc, exec, s[10:11]
	s_mov_b64 s[10:11], -1
	s_cbranch_vccnz .LBB0_1916
	v_and_b32_e32 v34, 0x1000, v130
	v_mov_b32_e32 v35, v155
	v_lshl_add_u64 v[34:35], s[12:13], 0, v[34:35]
	v_lshlrev_b32_e32 v36, 6, v98
	v_mov_b32_e32 v37, v155
	v_lshl_add_u64 v[34:35], v[34:35], 0, v[36:37]
	v_and_b32_e32 v36, 48, v175
	v_lshl_add_u64 v[34:35], v[34:35], 0, v[36:37]
	s_mov_b64 s[10:11], 0
	s_waitcnt lgkmcnt(1)
	global_store_dwordx4 v[34:35], v[6:9], off sc1
	s_waitcnt lgkmcnt(0)
	global_store_dwordx4 v[34:35], v[14:17], off offset:512 sc1
.LBB0_1916:
	s_andn2_b64 vcc, exec, s[10:11]
	s_cbranch_vccnz .LBB0_1918
	v_mov_b32_e32 v131, v155
	v_lshl_add_u64 v[34:35], s[12:13], 0, v[130:131]
	v_lshlrev_b32_e32 v36, 4, v98
	v_mov_b32_e32 v37, v155
	v_lshl_add_u64 v[34:35], v[34:35], 0, v[36:37]
	s_waitcnt lgkmcnt(1)
	global_store_dwordx4 v[34:35], v[6:9], off sc1
	s_waitcnt lgkmcnt(0)
	global_store_dwordx4 v[34:35], v[14:17], off offset:128 sc1

.LBB0_1924:
	s_add_i32 s14, s78, 16
	s_ashr_i32 s15, s14, 31
	s_lshl_b64 s[14:15], s[14:15], 11
	ds_write_b128 v162, v[106:109]
	ds_write_b128 v162, v[98:101] offset:64
	s_waitcnt lgkmcnt(3)
	v_add3_u32 v102, s19, v163, v118
	s_add_u32 s14, s77, s14
	ds_read_b128 v[98:101], v102
	ds_read_b128 v[102:105], v102 offset:1152
	s_addc_u32 s15, s16, s15
	v_lshl_add_u64 v[106:107], s[14:15], 0, v[154:155]
	v_mov_b32_e32 v119, v155
	v_lshl_add_u64 v[106:107], v[106:107], 0, v[118:119]
	s_waitcnt lgkmcnt(1)
	global_store_dwordx4 v[106:107], v[98:101], off sc1
	s_nop 1
	v_or_b32_e32 v98, 0x4000, v154
	v_mov_b32_e32 v99, v155
	v_lshl_add_u64 v[98:99], s[14:15], 0, v[98:99]
	v_lshl_add_u64 v[98:99], v[98:99], 0, v[118:119]
	s_waitcnt lgkmcnt(0)
	global_store_dwordx4 v[98:99], v[102:105], off sc1
	v_cndmask_b32_e64 v98, 0, 1, s[84:85]
	v_cmp_ne_u32_e64 s[14:15], 1, v98
	s_andn2_b64 vcc, exec, s[84:85]
	s_cbranch_vccz .LBB0_1872
	s_branch .LBB0_1873

.LBB0_1926:
	s_add_i32 s84, s78, 32
	s_ashr_i32 s85, s84, 31
	s_lshl_b64 s[84:85], s[84:85], 11
	ds_write_b128 v162, v[90:93]
	ds_write_b128 v162, v[82:85] offset:64
	s_waitcnt lgkmcnt(3)
	v_add3_u32 v86, s19, v163, v118
	s_add_u32 s84, s77, s84
	ds_read_b128 v[82:85], v86
	ds_read_b128 v[86:89], v86 offset:1152
	s_addc_u32 s85, s16, s85
	v_lshl_add_u64 v[90:91], s[84:85], 0, v[154:155]
	v_mov_b32_e32 v119, v155
	v_lshl_add_u64 v[90:91], v[90:91], 0, v[118:119]
	s_waitcnt lgkmcnt(1)
	global_store_dwordx4 v[90:91], v[82:85], off sc1
	s_nop 1
	v_or_b32_e32 v82, 0x4000, v154
	v_mov_b32_e32 v83, v155
	v_lshl_add_u64 v[82:83], s[84:85], 0, v[82:83]
	v_lshl_add_u64 v[82:83], v[82:83], 0, v[118:119]
	s_waitcnt lgkmcnt(0)
	global_store_dwordx4 v[82:83], v[86:89], off sc1
	s_and_b64 vcc, exec, s[14:15]
	s_cbranch_vccz .LBB0_1880
	s_branch .LBB0_1881

.LBB0_1928:
	s_add_i32 s84, s78, 48
	s_ashr_i32 s85, s84, 31
	s_lshl_b64 s[84:85], s[84:85], 11
	ds_write_b128 v162, v[74:77]
	ds_write_b128 v162, v[66:69] offset:64
	s_waitcnt lgkmcnt(3)
	v_add3_u32 v70, s19, v163, v118
	s_add_u32 s84, s77, s84
	ds_read_b128 v[66:69], v70
	ds_read_b128 v[70:73], v70 offset:1152
	s_addc_u32 s85, s16, s85
	v_lshl_add_u64 v[74:75], s[84:85], 0, v[154:155]
	v_mov_b32_e32 v119, v155
	v_lshl_add_u64 v[74:75], v[74:75], 0, v[118:119]
	s_waitcnt lgkmcnt(1)
	global_store_dwordx4 v[74:75], v[66:69], off sc1
	s_nop 1
	v_or_b32_e32 v66, 0x4000, v154
	v_mov_b32_e32 v67, v155
	v_lshl_add_u64 v[66:67], s[84:85], 0, v[66:67]
	v_lshl_add_u64 v[66:67], v[66:67], 0, v[118:119]
	s_waitcnt lgkmcnt(0)
	global_store_dwordx4 v[66:67], v[70:73], off sc1
	s_and_b64 vcc, exec, s[14:15]
	s_cbranch_vccz .LBB0_1888
	s_branch .LBB0_1889

.LBB0_1930:
	s_ashr_i32 s81, s80, 31
	s_lshl_b64 s[84:85], s[80:81], 11
	ds_write_b128 v162, v[58:61]
	ds_write_b128 v162, v[50:53] offset:64
	s_waitcnt lgkmcnt(3)
	v_add3_u32 v54, s19, v163, v118
	s_add_u32 s84, s77, s84
	ds_read_b128 v[50:53], v54
	ds_read_b128 v[54:57], v54 offset:1152
	s_addc_u32 s85, s16, s85
	v_lshl_add_u64 v[58:59], s[84:85], 0, v[154:155]
	v_mov_b32_e32 v119, v155
	v_lshl_add_u64 v[58:59], v[58:59], 0, v[118:119]
	s_waitcnt lgkmcnt(1)
	global_store_dwordx4 v[58:59], v[50:53], off sc1
	s_nop 1
	v_or_b32_e32 v50, 0x4000, v154
	v_mov_b32_e32 v51, v155
	v_lshl_add_u64 v[50:51], s[84:85], 0, v[50:51]
	v_lshl_add_u64 v[50:51], v[50:51], 0, v[118:119]
	s_waitcnt lgkmcnt(0)
	global_store_dwordx4 v[50:51], v[54:57], off sc1
	s_and_b64 vcc, exec, s[14:15]
	s_cbranch_vccz .LBB0_1896
	s_branch .LBB0_1897

.LBB0_1932:
	s_add_i32 s84, s78, 0x90
	s_ashr_i32 s85, s84, 31
	s_lshl_b64 s[84:85], s[84:85], 11
	ds_write_b128 v162, v[42:45]
	ds_write_b128 v162, v[34:37] offset:64
	s_waitcnt lgkmcnt(3)
	v_add3_u32 v38, s19, v163, v118
	s_add_u32 s84, s77, s84
	ds_read_b128 v[34:37], v38
	ds_read_b128 v[38:41], v38 offset:1152
	s_addc_u32 s85, s16, s85
	v_lshl_add_u64 v[42:43], s[84:85], 0, v[154:155]
	v_mov_b32_e32 v119, v155
	v_lshl_add_u64 v[42:43], v[42:43], 0, v[118:119]
	s_waitcnt lgkmcnt(1)
	global_store_dwordx4 v[42:43], v[34:37], off sc1
	s_nop 1
	v_or_b32_e32 v34, 0x4000, v154
	v_mov_b32_e32 v35, v155
	v_lshl_add_u64 v[34:35], s[84:85], 0, v[34:35]
	v_lshl_add_u64 v[34:35], v[34:35], 0, v[118:119]
	s_waitcnt lgkmcnt(0)
	global_store_dwordx4 v[34:35], v[38:41], off sc1
	s_and_b64 vcc, exec, s[14:15]
	s_cbranch_vccz .LBB0_1904
	s_branch .LBB0_1905

.LBB0_1934:
	s_add_i32 s84, s78, 0xa0
	s_ashr_i32 s85, s84, 31
	s_lshl_b64 s[84:85], s[84:85], 11
	ds_write_b128 v162, v[26:29]
	ds_write_b128 v162, v[18:21] offset:64
	s_waitcnt lgkmcnt(3)
	v_add3_u32 v22, s19, v163, v118
	s_add_u32 s84, s77, s84
	ds_read_b128 v[18:21], v22
	ds_read_b128 v[22:25], v22 offset:1152
	s_addc_u32 s85, s16, s85
	v_lshl_add_u64 v[26:27], s[84:85], 0, v[154:155]
	v_mov_b32_e32 v119, v155
	v_lshl_add_u64 v[26:27], v[26:27], 0, v[118:119]
	s_waitcnt lgkmcnt(1)
	global_store_dwordx4 v[26:27], v[18:21], off sc1
	s_nop 1
	v_or_b32_e32 v18, 0x4000, v154
	v_mov_b32_e32 v19, v155
	v_lshl_add_u64 v[18:19], s[84:85], 0, v[18:19]
	v_lshl_add_u64 v[18:19], v[18:19], 0, v[118:119]
	s_waitcnt lgkmcnt(0)
	global_store_dwordx4 v[18:19], v[22:25], off sc1
	s_and_b64 vcc, exec, s[14:15]
	s_cbranch_vccz .LBB0_1912
	s_branch .LBB0_1913

.LBB0_1936:
	s_add_i32 s10, s78, 0xb0
	s_ashr_i32 s11, s10, 31
	s_lshl_b64 s[10:11], s[10:11], 11
	ds_write_b128 v162, v[10:13]
	ds_write_b128 v162, v[2:5] offset:64
	s_waitcnt lgkmcnt(3)
	v_add3_u32 v6, s19, v163, v118
	s_add_u32 s10, s77, s10
	ds_read_b128 v[2:5], v6
	ds_read_b128 v[6:9], v6 offset:1152
	s_addc_u32 s11, s16, s11
	v_lshl_add_u64 v[10:11], s[10:11], 0, v[154:155]
	v_mov_b32_e32 v119, v155
	v_lshl_add_u64 v[10:11], v[10:11], 0, v[118:119]
	v_or_b32_e32 v154, 0x4000, v154
	s_waitcnt lgkmcnt(1)
	global_store_dwordx4 v[10:11], v[2:5], off sc1
	s_nop 1
	v_lshl_add_u64 v[2:3], s[10:11], 0, v[154:155]
	v_lshl_add_u64 v[2:3], v[2:3], 0, v[118:119]
	s_waitcnt lgkmcnt(0)
	global_store_dwordx4 v[2:3], v[6:9], off sc1
	s_and_b64 vcc, exec, s[14:15]
	s_cbranch_vccz .LBB0_1920
